# grid barrier cross-XCD hop: waiting XCD leaders poll the monotonic arrival counter TOP for (tg+1)*nx (target kept in an SGPR) instead of TOPGEN, which the last leader bumps only after its own TOP atom
# speedup vs baseline: 1.0083x; 1.0033x over previous
.LBB0_207:
	s_or_b64 exec, exec, s[6:7]
	v_cvt_f32_u32_e32 v3, v0
	s_waitcnt vmcnt(0)
	v_readfirstlane_b32 s4, v2
	s_add_u32 s6, s72, 0x3500
	s_addc_u32 s7, s73, 0
	v_rcp_iflag_f32_e32 v3, v3
	v_add_u32_e32 v1, s4, v1
	v_add_u32_e32 v4, 1, v1
	s_mov_b64 s[8:9], -1
	v_mul_f32_e32 v2, 0x4f7ffffe, v3
	v_cvt_u32_f32_e32 v2, v2
	v_sub_u32_e32 v3, 0, v0
	v_mul_lo_u32 v3, v3, v2
	v_mul_hi_u32 v3, v2, v3
	v_add_u32_e32 v2, v2, v3
	v_mul_hi_u32 v2, v1, v2
	v_mul_lo_u32 v3, v2, v0
	v_sub_u32_e32 v1, v1, v3
	v_add_u32_e32 v5, 1, v2
	v_cmp_ge_u32_e32 vcc, v1, v0
	v_sub_u32_e32 v3, v1, v0
	s_nop 0
	v_cndmask_b32_e32 v2, v2, v5, vcc
	v_cndmask_b32_e32 v1, v1, v3, vcc
	v_add_u32_e32 v3, 1, v2
	v_cmp_ge_u32_e32 vcc, v1, v0
	s_nop 1
	v_cndmask_b32_e32 v2, v2, v3, vcc
	v_mul_lo_u32 v1, v0, v2
	v_add_u32_e32 v0, v1, v0
	v_cmp_ne_u32_e32 vcc, v4, v0
	v_readfirstlane_b32 s98, v0
	v_mov_b64_e32 v[0:1], s[6:7]
	s_and_saveexec_b64 s[4:5], vcc
	s_cbranch_execz .LBB0_219
	v_mov_b32_e32 v0, 0
	global_load_dword v1, v0, s[6:7] offset:-256 sc1
	s_mov_b64 s[12:13], 0
	s_waitcnt vmcnt(0)
	v_cmp_gt_u32_e32 vcc, s98, v1
	s_and_saveexec_b64 s[10:11], vcc
	s_cbranch_execz .LBB0_218
	s_add_u32 s8, s72, 0x200
	s_addc_u32 s9, s73, 0
	s_mov_b32 s16, 1
	s_branch .LBB0_211

.LBB0_213:
	global_load_dword v1, v0, s[6:7] offset:-256 sc1
	s_add_i32 s16, s16, 1
	s_mov_b64 s[34:35], -1
	s_waitcnt vmcnt(0)
	v_cmp_le_u32_e32 vcc, s98, v1
	s_orn2_b64 s[38:39], vcc, exec
	s_branch .LBB0_210

.LBB0_283:
	s_or_b64 exec, exec, s[8:9]
	v_cvt_f32_u32_e32 v3, v0
	s_waitcnt vmcnt(0)
	v_readfirstlane_b32 s6, v2
	s_add_u32 s8, s72, 0x3500
	s_addc_u32 s9, s73, 0
	v_rcp_iflag_f32_e32 v3, v3
	v_add_u32_e32 v1, s6, v1
	v_add_u32_e32 v4, 1, v1
	s_mov_b64 s[10:11], -1
	v_mul_f32_e32 v2, 0x4f7ffffe, v3
	v_cvt_u32_f32_e32 v2, v2
	v_sub_u32_e32 v3, 0, v0
	v_mul_lo_u32 v3, v3, v2
	v_mul_hi_u32 v3, v2, v3
	v_add_u32_e32 v2, v2, v3
	v_mul_hi_u32 v2, v1, v2
	v_mul_lo_u32 v3, v2, v0
	v_sub_u32_e32 v1, v1, v3
	v_add_u32_e32 v5, 1, v2
	v_cmp_ge_u32_e32 vcc, v1, v0
	v_sub_u32_e32 v3, v1, v0
	s_nop 0
	v_cndmask_b32_e32 v2, v2, v5, vcc
	v_cndmask_b32_e32 v1, v1, v3, vcc
	v_add_u32_e32 v3, 1, v2
	v_cmp_ge_u32_e32 vcc, v1, v0
	s_nop 1
	v_cndmask_b32_e32 v2, v2, v3, vcc
	v_mul_lo_u32 v1, v0, v2
	v_add_u32_e32 v0, v1, v0
	v_cmp_ne_u32_e32 vcc, v4, v0
	v_readfirstlane_b32 s98, v0
	v_mov_b64_e32 v[0:1], s[8:9]
	s_and_saveexec_b64 s[6:7], vcc
	s_cbranch_execz .LBB0_295
	v_mov_b32_e32 v0, 0
	global_load_dword v1, v0, s[8:9] offset:-256 sc1
	s_mov_b64 s[14:15], 0
	s_waitcnt vmcnt(0)
	v_cmp_gt_u32_e32 vcc, s98, v1
	s_and_saveexec_b64 s[12:13], vcc
	s_cbranch_execz .LBB0_294
	s_add_u32 s10, s72, 0x200
	s_addc_u32 s11, s73, 0
	s_mov_b32 s16, 1
	s_branch .LBB0_287

.LBB0_289:
	global_load_dword v1, v0, s[8:9] offset:-256 sc1
	s_add_i32 s16, s16, 1
	s_mov_b64 s[36:37], -1
	s_waitcnt vmcnt(0)
	v_cmp_le_u32_e32 vcc, s98, v1
	s_orn2_b64 s[40:41], vcc, exec
	s_branch .LBB0_286

.LBB0_559:
	global_load_dword v1, v0, s[6:7] offset:-256 sc1
	s_add_i32 s16, s16, 1
	s_mov_b64 s[24:25], -1
	s_waitcnt vmcnt(0)
	v_cmp_le_u32_e32 vcc, s98, v1
	s_orn2_b64 s[34:35], vcc, exec
	s_branch .LBB0_556

.LBB0_707:
	s_or_b64 exec, exec, s[6:7]
	v_cvt_f32_u32_e32 v3, v0
	s_waitcnt vmcnt(0)
	v_readfirstlane_b32 s4, v2
	s_add_u32 s6, s72, 0x3500
	s_addc_u32 s7, s73, 0
	v_rcp_iflag_f32_e32 v3, v3
	v_add_u32_e32 v1, s4, v1
	v_add_u32_e32 v4, 1, v1
	s_mov_b64 s[10:11], -1
	v_mul_f32_e32 v2, 0x4f7ffffe, v3
	v_cvt_u32_f32_e32 v2, v2
	v_sub_u32_e32 v3, 0, v0
	v_mul_lo_u32 v3, v3, v2
	v_mul_hi_u32 v3, v2, v3
	v_add_u32_e32 v2, v2, v3
	v_mul_hi_u32 v2, v1, v2
	v_mul_lo_u32 v3, v2, v0
	v_sub_u32_e32 v1, v1, v3
	v_add_u32_e32 v5, 1, v2
	v_cmp_ge_u32_e32 vcc, v1, v0
	v_sub_u32_e32 v3, v1, v0
	s_nop 0
	v_cndmask_b32_e32 v2, v2, v5, vcc
	v_cndmask_b32_e32 v1, v1, v3, vcc
	v_add_u32_e32 v3, 1, v2
	v_cmp_ge_u32_e32 vcc, v1, v0
	s_nop 1
	v_cndmask_b32_e32 v2, v2, v3, vcc
	v_mul_lo_u32 v1, v0, v2
	v_add_u32_e32 v0, v1, v0
	v_cmp_ne_u32_e32 vcc, v4, v0
	v_readfirstlane_b32 s98, v0
	v_mov_b64_e32 v[0:1], s[6:7]
	s_and_saveexec_b64 s[4:5], vcc
	s_cbranch_execz .LBB0_719
	v_mov_b32_e32 v0, 0
	global_load_dword v1, v0, s[6:7] offset:-256 sc1
	s_mov_b64 s[14:15], 0
	s_waitcnt vmcnt(0)
	v_cmp_gt_u32_e32 vcc, s98, v1
	s_and_saveexec_b64 s[12:13], vcc
	s_cbranch_execz .LBB0_718
	s_add_u32 s10, s72, 0x200
	s_addc_u32 s11, s73, 0
	s_mov_b32 s18, 1
	s_branch .LBB0_711

.LBB0_713:
	global_load_dword v1, v0, s[6:7] offset:-256 sc1
	s_add_i32 s18, s18, 1
	s_mov_b64 s[24:25], -1
	s_waitcnt vmcnt(0)
	v_cmp_le_u32_e32 vcc, s98, v1
	s_orn2_b64 s[34:35], vcc, exec
	s_branch .LBB0_710

.LBB0_777:
	s_or_b64 exec, exec, s[6:7]
	v_cvt_f32_u32_e32 v3, v0
	s_waitcnt vmcnt(0)
	v_readfirstlane_b32 s4, v2
	s_add_u32 s6, s72, 0x3500
	s_addc_u32 s7, s73, 0
	v_rcp_iflag_f32_e32 v3, v3
	v_add_u32_e32 v1, s4, v1
	v_add_u32_e32 v4, 1, v1
	s_mov_b64 s[12:13], -1
	v_mul_f32_e32 v2, 0x4f7ffffe, v3
	v_cvt_u32_f32_e32 v2, v2
	v_sub_u32_e32 v3, 0, v0
	v_mul_lo_u32 v3, v3, v2
	v_mul_hi_u32 v3, v2, v3
	v_add_u32_e32 v2, v2, v3
	v_mul_hi_u32 v2, v1, v2
	v_mul_lo_u32 v3, v2, v0
	v_sub_u32_e32 v1, v1, v3
	v_add_u32_e32 v5, 1, v2
	v_cmp_ge_u32_e32 vcc, v1, v0
	v_sub_u32_e32 v3, v1, v0
	s_nop 0
	v_cndmask_b32_e32 v2, v2, v5, vcc
	v_cndmask_b32_e32 v1, v1, v3, vcc
	v_add_u32_e32 v3, 1, v2
	v_cmp_ge_u32_e32 vcc, v1, v0
	s_nop 1
	v_cndmask_b32_e32 v2, v2, v3, vcc
	v_mul_lo_u32 v1, v0, v2
	v_add_u32_e32 v0, v1, v0
	v_cmp_ne_u32_e32 vcc, v4, v0
	v_readfirstlane_b32 s98, v0
	v_mov_b64_e32 v[0:1], s[6:7]
	s_and_saveexec_b64 s[4:5], vcc
	s_cbranch_execz .LBB0_789
	v_mov_b32_e32 v0, 0
	global_load_dword v1, v0, s[6:7] offset:-256 sc1
	s_mov_b64 s[16:17], 0
	s_waitcnt vmcnt(0)
	v_cmp_gt_u32_e32 vcc, s98, v1
	s_and_saveexec_b64 s[14:15], vcc
	s_cbranch_execz .LBB0_788
	s_add_u32 s12, s72, 0x200
	s_addc_u32 s13, s73, 0
	s_mov_b32 s18, 1
	s_branch .LBB0_781

.LBB0_783:
	global_load_dword v1, v0, s[6:7] offset:-256 sc1
	s_add_i32 s18, s18, 1
	s_mov_b64 s[26:27], -1
	s_waitcnt vmcnt(0)
	v_cmp_le_u32_e32 vcc, s98, v1
	s_orn2_b64 s[36:37], vcc, exec
	s_branch .LBB0_780

.LBB0_875:
	s_or_b64 exec, exec, s[12:13]
	v_cvt_f32_u32_e32 v3, v0
	s_waitcnt vmcnt(0)
	v_readfirstlane_b32 s4, v2
	s_add_u32 s12, s72, 0x3500
	s_addc_u32 s13, s73, 0
	v_rcp_iflag_f32_e32 v3, v3
	v_add_u32_e32 v1, s4, v1
	v_add_u32_e32 v4, 1, v1
	s_mov_b64 s[14:15], -1
	v_mul_f32_e32 v2, 0x4f7ffffe, v3
	v_cvt_u32_f32_e32 v2, v2
	v_sub_u32_e32 v3, 0, v0
	v_mul_lo_u32 v3, v3, v2
	v_mul_hi_u32 v3, v2, v3
	v_add_u32_e32 v2, v2, v3
	v_mul_hi_u32 v2, v1, v2
	v_mul_lo_u32 v3, v2, v0
	v_sub_u32_e32 v1, v1, v3
	v_add_u32_e32 v5, 1, v2
	v_cmp_ge_u32_e32 vcc, v1, v0
	v_sub_u32_e32 v3, v1, v0
	s_nop 0
	v_cndmask_b32_e32 v2, v2, v5, vcc
	v_cndmask_b32_e32 v1, v1, v3, vcc
	v_add_u32_e32 v3, 1, v2
	v_cmp_ge_u32_e32 vcc, v1, v0
	s_nop 1
	v_cndmask_b32_e32 v2, v2, v3, vcc
	v_mul_lo_u32 v1, v0, v2
	v_add_u32_e32 v0, v1, v0
	v_cmp_ne_u32_e32 vcc, v4, v0
	v_readfirstlane_b32 s98, v0
	v_mov_b64_e32 v[0:1], s[12:13]
	s_and_saveexec_b64 s[4:5], vcc
	s_cbranch_execz .LBB0_887
	v_mov_b32_e32 v0, 0
	global_load_dword v1, v0, s[12:13] offset:-256 sc1
	s_mov_b64 s[24:25], 0
	s_waitcnt vmcnt(0)
	v_cmp_gt_u32_e32 vcc, s98, v1
	s_and_saveexec_b64 s[16:17], vcc
	s_cbranch_execz .LBB0_886
	s_add_u32 s14, s72, 0x200
	s_addc_u32 s15, s73, 0
	s_mov_b32 s18, 1
	s_branch .LBB0_879

.LBB0_881:
	global_load_dword v1, v0, s[12:13] offset:-256 sc1
	s_add_i32 s18, s18, 1
	s_mov_b64 s[34:35], -1
	s_waitcnt vmcnt(0)
	v_cmp_le_u32_e32 vcc, s98, v1
	s_orn2_b64 s[38:39], vcc, exec
	s_branch .LBB0_878

.LBB0_965:
	s_or_b64 exec, exec, s[12:13]
	v_cvt_f32_u32_e32 v3, v0
	s_waitcnt vmcnt(0)
	v_readfirstlane_b32 s6, v2
	s_add_u32 s12, s72, 0x3500
	s_addc_u32 s13, s73, 0
	v_rcp_iflag_f32_e32 v3, v3
	v_add_u32_e32 v1, s6, v1
	v_add_u32_e32 v4, 1, v1
	s_mov_b64 s[14:15], -1
	v_mul_f32_e32 v2, 0x4f7ffffe, v3
	v_cvt_u32_f32_e32 v2, v2
	v_sub_u32_e32 v3, 0, v0
	v_mul_lo_u32 v3, v3, v2
	v_mul_hi_u32 v3, v2, v3
	v_add_u32_e32 v2, v2, v3
	v_mul_hi_u32 v2, v1, v2
	v_mul_lo_u32 v3, v2, v0
	v_sub_u32_e32 v1, v1, v3
	v_add_u32_e32 v5, 1, v2
	v_cmp_ge_u32_e32 vcc, v1, v0
	v_sub_u32_e32 v3, v1, v0
	s_nop 0
	v_cndmask_b32_e32 v2, v2, v5, vcc
	v_cndmask_b32_e32 v1, v1, v3, vcc
	v_add_u32_e32 v3, 1, v2
	v_cmp_ge_u32_e32 vcc, v1, v0
	s_nop 1
	v_cndmask_b32_e32 v2, v2, v3, vcc
	v_mul_lo_u32 v1, v0, v2
	v_add_u32_e32 v0, v1, v0
	v_cmp_ne_u32_e32 vcc, v4, v0
	v_readfirstlane_b32 s98, v0
	v_mov_b64_e32 v[0:1], s[12:13]
	s_and_saveexec_b64 s[6:7], vcc
	s_cbranch_execz .LBB0_977
	v_mov_b32_e32 v0, 0
	global_load_dword v1, v0, s[12:13] offset:-256 sc1
	s_mov_b64 s[24:25], 0
	s_waitcnt vmcnt(0)
	v_cmp_gt_u32_e32 vcc, s98, v1
	s_and_saveexec_b64 s[16:17], vcc
	s_cbranch_execz .LBB0_976
	s_add_u32 s14, s72, 0x200
	s_addc_u32 s15, s73, 0
	s_mov_b32 s18, 1
	s_branch .LBB0_969

.LBB0_1145:
	s_or_b64 exec, exec, s[6:7]
	v_cvt_f32_u32_e32 v3, v0
	s_waitcnt vmcnt(0)
	v_readfirstlane_b32 s4, v2
	s_add_u32 s6, s72, 0x3500
	s_addc_u32 s7, s73, 0
	v_rcp_iflag_f32_e32 v3, v3
	v_add_u32_e32 v1, s4, v1
	v_add_u32_e32 v4, 1, v1
	s_mov_b64 s[8:9], -1
	v_mul_f32_e32 v2, 0x4f7ffffe, v3
	v_cvt_u32_f32_e32 v2, v2
	v_sub_u32_e32 v3, 0, v0
	v_mul_lo_u32 v3, v3, v2
	v_mul_hi_u32 v3, v2, v3
	v_add_u32_e32 v2, v2, v3
	v_mul_hi_u32 v2, v1, v2
	v_mul_lo_u32 v3, v2, v0
	v_sub_u32_e32 v1, v1, v3
	v_add_u32_e32 v5, 1, v2
	v_cmp_ge_u32_e32 vcc, v1, v0
	v_sub_u32_e32 v3, v1, v0
	s_nop 0
	v_cndmask_b32_e32 v2, v2, v5, vcc
	v_cndmask_b32_e32 v1, v1, v3, vcc
	v_add_u32_e32 v3, 1, v2
	v_cmp_ge_u32_e32 vcc, v1, v0
	s_nop 1
	v_cndmask_b32_e32 v2, v2, v3, vcc
	v_mul_lo_u32 v1, v0, v2
	v_add_u32_e32 v0, v1, v0
	v_cmp_ne_u32_e32 vcc, v4, v0
	v_readfirstlane_b32 s98, v0
	v_mov_b64_e32 v[0:1], s[6:7]
	s_and_saveexec_b64 s[4:5], vcc
	s_cbranch_execz .LBB0_1157
	v_mov_b32_e32 v0, 0
	global_load_dword v1, v0, s[6:7] offset:-256 sc1
	s_mov_b64 s[12:13], 0
	s_waitcnt vmcnt(0)
	v_cmp_gt_u32_e32 vcc, s98, v1
	s_and_saveexec_b64 s[10:11], vcc
	s_cbranch_execz .LBB0_1156
	s_add_u32 s8, s72, 0x200
	s_addc_u32 s9, s73, 0
	s_mov_b32 s18, 1
	s_branch .LBB0_1149

.LBB0_1151:
	global_load_dword v1, v0, s[6:7] offset:-256 sc1
	s_add_i32 s18, s18, 1
	s_mov_b64 s[16:17], -1
	s_waitcnt vmcnt(0)
	v_cmp_le_u32_e32 vcc, s98, v1
	s_orn2_b64 s[26:27], vcc, exec
	s_branch .LBB0_1148

.LBB0_1590:
	global_load_dword v1, v0, s[6:7] offset:-256 sc1
	s_add_i32 s18, s18, 1
	s_mov_b64 s[16:17], -1
	s_waitcnt vmcnt(0)
	v_cmp_le_u32_e32 vcc, s98, v1
	s_orn2_b64 s[30:31], vcc, exec
	s_branch .LBB0_1587

.LBB0_1660:
	global_load_dword v1, v0, s[6:7] offset:-256 sc1
	s_add_i32 s18, s18, 1
	s_mov_b64 s[16:17], -1
	s_waitcnt vmcnt(0)
	v_cmp_le_u32_e32 vcc, s98, v1
	s_orn2_b64 s[34:35], vcc, exec
	s_branch .LBB0_1657

.LBB0_1752:
	s_or_b64 exec, exec, s[8:9]
	v_cvt_f32_u32_e32 v3, v0
	s_waitcnt vmcnt(0)
	v_readfirstlane_b32 s4, v2
	s_add_u32 s8, s72, 0x3500
	s_addc_u32 s9, s73, 0
	v_rcp_iflag_f32_e32 v3, v3
	v_add_u32_e32 v1, s4, v1
	v_add_u32_e32 v4, 1, v1
	s_mov_b64 s[10:11], -1
	v_mul_f32_e32 v2, 0x4f7ffffe, v3
	v_cvt_u32_f32_e32 v2, v2
	v_sub_u32_e32 v3, 0, v0
	v_mul_lo_u32 v3, v3, v2
	v_mul_hi_u32 v3, v2, v3
	v_add_u32_e32 v2, v2, v3
	v_mul_hi_u32 v2, v1, v2
	v_mul_lo_u32 v3, v2, v0
	v_sub_u32_e32 v1, v1, v3
	v_add_u32_e32 v5, 1, v2
	v_cmp_ge_u32_e32 vcc, v1, v0
	v_sub_u32_e32 v3, v1, v0
	s_nop 0
	v_cndmask_b32_e32 v2, v2, v5, vcc
	v_cndmask_b32_e32 v1, v1, v3, vcc
	v_add_u32_e32 v3, 1, v2
	v_cmp_ge_u32_e32 vcc, v1, v0
	s_nop 1
	v_cndmask_b32_e32 v2, v2, v3, vcc
	v_mul_lo_u32 v1, v0, v2
	v_add_u32_e32 v0, v1, v0
	v_cmp_ne_u32_e32 vcc, v4, v0
	v_readfirstlane_b32 s98, v0
	v_mov_b64_e32 v[0:1], s[8:9]
	s_and_saveexec_b64 s[4:5], vcc
	s_cbranch_execz .LBB0_1764
	v_mov_b32_e32 v0, 0
	global_load_dword v1, v0, s[8:9] offset:-256 sc1
	s_mov_b64 s[14:15], 0
	s_waitcnt vmcnt(0)
	v_cmp_gt_u32_e32 vcc, s98, v1
	s_and_saveexec_b64 s[12:13], vcc
	s_cbranch_execz .LBB0_1763
	s_add_u32 s10, s72, 0x200
	s_addc_u32 s11, s73, 0
	s_mov_b32 s18, 1
	s_branch .LBB0_1756

.LBB0_1758:
	global_load_dword v1, v0, s[8:9] offset:-256 sc1
	s_add_i32 s18, s18, 1
	s_mov_b64 s[30:31], -1
	s_waitcnt vmcnt(0)
	v_cmp_le_u32_e32 vcc, s98, v1
	s_orn2_b64 s[36:37], vcc, exec
	s_branch .LBB0_1755

.LBB0_1842:
	s_or_b64 exec, exec, s[8:9]
	v_cvt_f32_u32_e32 v3, v0
	s_waitcnt vmcnt(0)
	v_readfirstlane_b32 s6, v2
	s_add_u32 s8, s72, 0x3500
	s_addc_u32 s9, s73, 0
	v_rcp_iflag_f32_e32 v3, v3
	v_add_u32_e32 v1, s6, v1
	v_add_u32_e32 v4, 1, v1
	s_mov_b64 s[10:11], -1
	v_mul_f32_e32 v2, 0x4f7ffffe, v3
	v_cvt_u32_f32_e32 v2, v2
	v_sub_u32_e32 v3, 0, v0
	v_mul_lo_u32 v3, v3, v2
	v_mul_hi_u32 v3, v2, v3
	v_add_u32_e32 v2, v2, v3
	v_mul_hi_u32 v2, v1, v2
	v_mul_lo_u32 v3, v2, v0
	v_sub_u32_e32 v1, v1, v3
	v_add_u32_e32 v5, 1, v2
	v_cmp_ge_u32_e32 vcc, v1, v0
	v_sub_u32_e32 v3, v1, v0
	s_nop 0
	v_cndmask_b32_e32 v2, v2, v5, vcc
	v_cndmask_b32_e32 v1, v1, v3, vcc
	v_add_u32_e32 v3, 1, v2
	v_cmp_ge_u32_e32 vcc, v1, v0
	s_nop 1
	v_cndmask_b32_e32 v2, v2, v3, vcc
	v_mul_lo_u32 v1, v0, v2
	v_add_u32_e32 v0, v1, v0
	v_cmp_ne_u32_e32 vcc, v4, v0
	v_readfirstlane_b32 s98, v0
	v_mov_b64_e32 v[0:1], s[8:9]
	s_and_saveexec_b64 s[6:7], vcc
	s_cbranch_execz .LBB0_1854
	v_mov_b32_e32 v0, 0
	global_load_dword v1, v0, s[8:9] offset:-256 sc1
	s_mov_b64 s[14:15], 0
	s_waitcnt vmcnt(0)
	v_cmp_gt_u32_e32 vcc, s98, v1
	s_and_saveexec_b64 s[12:13], vcc
	s_cbranch_execz .LBB0_1853
	s_add_u32 s10, s72, 0x200
	s_addc_u32 s11, s73, 0
	s_mov_b32 s18, 1
	s_branch .LBB0_1846

.LBB0_2344:
	s_or_b64 exec, exec, s[6:7]
	v_cvt_f32_u32_e32 v3, v0
	s_waitcnt vmcnt(0)
	v_readfirstlane_b32 s4, v2
	s_add_u32 s6, s72, 0x3500
	s_addc_u32 s7, s73, 0
	v_rcp_iflag_f32_e32 v3, v3
	v_add_u32_e32 v1, s4, v1
	v_add_u32_e32 v4, 1, v1
	s_mov_b64 s[8:9], -1
	v_mul_f32_e32 v2, 0x4f7ffffe, v3
	v_cvt_u32_f32_e32 v2, v2
	v_sub_u32_e32 v3, 0, v0
	v_mul_lo_u32 v3, v3, v2
	v_mul_hi_u32 v3, v2, v3
	v_add_u32_e32 v2, v2, v3
	v_mul_hi_u32 v2, v1, v2
	v_mul_lo_u32 v3, v2, v0
	v_sub_u32_e32 v1, v1, v3
	v_add_u32_e32 v5, 1, v2
	v_cmp_ge_u32_e32 vcc, v1, v0
	v_sub_u32_e32 v3, v1, v0
	s_nop 0
	v_cndmask_b32_e32 v2, v2, v5, vcc
	v_cndmask_b32_e32 v1, v1, v3, vcc
	v_add_u32_e32 v3, 1, v2
	v_cmp_ge_u32_e32 vcc, v1, v0
	s_nop 1
	v_cndmask_b32_e32 v2, v2, v3, vcc
	v_mul_lo_u32 v1, v0, v2
	v_add_u32_e32 v0, v1, v0
	v_cmp_ne_u32_e32 vcc, v4, v0
	v_readfirstlane_b32 s98, v0
	v_mov_b64_e32 v[0:1], s[6:7]
	s_and_saveexec_b64 s[4:5], vcc
	s_cbranch_execz .LBB0_2356
	v_mov_b32_e32 v0, 0
	global_load_dword v1, v0, s[6:7] offset:-256 sc1
	s_mov_b64 s[12:13], 0
	s_waitcnt vmcnt(0)
	v_cmp_gt_u32_e32 vcc, s98, v1
	s_and_saveexec_b64 s[10:11], vcc
	s_cbranch_execz .LBB0_2355
	s_add_u32 s8, s72, 0x200
	s_addc_u32 s9, s73, 0
	s_mov_b32 s22, 1
	s_branch .LBB0_2348

.LBB0_2350:
	global_load_dword v1, v0, s[6:7] offset:-256 sc1
	s_add_i32 s22, s22, 1
	s_mov_b64 s[16:17], -1
	s_waitcnt vmcnt(0)
	v_cmp_le_u32_e32 vcc, s98, v1
	s_orn2_b64 s[20:21], vcc, exec
	s_branch .LBB0_2347

.LBB0_2463:
	s_or_b64 exec, exec, s[6:7]
	v_cvt_f32_u32_e32 v3, v0
	s_waitcnt vmcnt(0)
	v_readfirstlane_b32 s4, v2
	s_add_u32 s6, s72, 0x3500
	s_addc_u32 s7, s73, 0
	v_rcp_iflag_f32_e32 v3, v3
	v_add_u32_e32 v1, s4, v1
	v_add_u32_e32 v4, 1, v1
	s_mov_b64 s[8:9], -1
	v_mul_f32_e32 v2, 0x4f7ffffe, v3
	v_cvt_u32_f32_e32 v2, v2
	v_sub_u32_e32 v3, 0, v0
	v_mul_lo_u32 v3, v3, v2
	v_mul_hi_u32 v3, v2, v3
	v_add_u32_e32 v2, v2, v3
	v_mul_hi_u32 v2, v1, v2
	v_mul_lo_u32 v3, v2, v0
	v_sub_u32_e32 v1, v1, v3
	v_add_u32_e32 v5, 1, v2
	v_cmp_ge_u32_e32 vcc, v1, v0
	v_sub_u32_e32 v3, v1, v0
	s_nop 0
	v_cndmask_b32_e32 v2, v2, v5, vcc
	v_cndmask_b32_e32 v1, v1, v3, vcc
	v_add_u32_e32 v3, 1, v2
	v_cmp_ge_u32_e32 vcc, v1, v0
	s_nop 1
	v_cndmask_b32_e32 v2, v2, v3, vcc
	v_mul_lo_u32 v1, v0, v2
	v_add_u32_e32 v0, v1, v0
	v_cmp_ne_u32_e32 vcc, v4, v0
	v_readfirstlane_b32 s98, v0
	v_mov_b64_e32 v[0:1], s[6:7]
	s_and_saveexec_b64 s[4:5], vcc
	s_cbranch_execz .LBB0_2475
	v_mov_b32_e32 v0, 0
	global_load_dword v1, v0, s[6:7] offset:-256 sc1
	s_mov_b64 s[12:13], 0
	s_waitcnt vmcnt(0)
	v_cmp_gt_u32_e32 vcc, s98, v1
	s_and_saveexec_b64 s[10:11], vcc
	s_cbranch_execz .LBB0_2474
	s_add_u32 s8, s72, 0x200
	s_addc_u32 s9, s73, 0
	s_mov_b32 s26, 1
	s_branch .LBB0_2467

.LBB0_2469:
	global_load_dword v1, v0, s[6:7] offset:-256 sc1
	s_add_i32 s26, s26, 1
	s_mov_b64 s[16:17], -1
	s_waitcnt vmcnt(0)
	v_cmp_le_u32_e32 vcc, s98, v1
	s_orn2_b64 s[24:25], vcc, exec
	s_branch .LBB0_2466

.LBB0_2533:
	s_or_b64 exec, exec, s[6:7]
	v_cvt_f32_u32_e32 v3, v0
	s_waitcnt vmcnt(0)
	v_readfirstlane_b32 s4, v2
	s_add_u32 s6, s72, 0x3500
	s_addc_u32 s7, s73, 0
	v_rcp_iflag_f32_e32 v3, v3
	v_add_u32_e32 v1, s4, v1
	v_add_u32_e32 v4, 1, v1
	s_mov_b64 s[8:9], -1
	v_mul_f32_e32 v2, 0x4f7ffffe, v3
	v_cvt_u32_f32_e32 v2, v2
	v_sub_u32_e32 v3, 0, v0
	v_mul_lo_u32 v3, v3, v2
	v_mul_hi_u32 v3, v2, v3
	v_add_u32_e32 v2, v2, v3
	v_mul_hi_u32 v2, v1, v2
	v_mul_lo_u32 v3, v2, v0
	v_sub_u32_e32 v1, v1, v3
	v_add_u32_e32 v5, 1, v2
	v_cmp_ge_u32_e32 vcc, v1, v0
	v_sub_u32_e32 v3, v1, v0
	s_nop 0
	v_cndmask_b32_e32 v2, v2, v5, vcc
	v_cndmask_b32_e32 v1, v1, v3, vcc
	v_add_u32_e32 v3, 1, v2
	v_cmp_ge_u32_e32 vcc, v1, v0
	s_nop 1
	v_cndmask_b32_e32 v2, v2, v3, vcc
	v_mul_lo_u32 v1, v0, v2
	v_add_u32_e32 v0, v1, v0
	v_cmp_ne_u32_e32 vcc, v4, v0
	v_readfirstlane_b32 s98, v0
	v_mov_b64_e32 v[0:1], s[6:7]
	s_and_saveexec_b64 s[4:5], vcc
	s_cbranch_execz .LBB0_2545
	v_mov_b32_e32 v0, 0
	global_load_dword v1, v0, s[6:7] offset:-256 sc1
	s_mov_b64 s[12:13], 0
	s_waitcnt vmcnt(0)
	v_cmp_gt_u32_e32 vcc, s98, v1
	s_and_saveexec_b64 s[10:11], vcc
	s_cbranch_execz .LBB0_2544
	s_add_u32 s8, s72, 0x200
	s_addc_u32 s9, s73, 0
	s_mov_b32 s28, 1
	s_branch .LBB0_2537

.LBB0_2539:
	global_load_dword v1, v0, s[6:7] offset:-256 sc1
	s_add_i32 s28, s28, 1
	s_mov_b64 s[16:17], -1
	s_waitcnt vmcnt(0)
	v_cmp_le_u32_e32 vcc, s98, v1
	s_orn2_b64 s[26:27], vcc, exec
	s_branch .LBB0_2536

.LBB0_2631:
	s_or_b64 exec, exec, s[8:9]
	v_cvt_f32_u32_e32 v3, v0
	s_waitcnt vmcnt(0)
	v_readfirstlane_b32 s4, v2
	s_add_u32 s8, s72, 0x3500
	s_addc_u32 s9, s73, 0
	v_rcp_iflag_f32_e32 v3, v3
	v_add_u32_e32 v1, s4, v1
	v_add_u32_e32 v4, 1, v1
	s_mov_b64 s[10:11], -1
	v_mul_f32_e32 v2, 0x4f7ffffe, v3
	v_cvt_u32_f32_e32 v2, v2
	v_sub_u32_e32 v3, 0, v0
	v_mul_lo_u32 v3, v3, v2
	v_mul_hi_u32 v3, v2, v3
	v_add_u32_e32 v2, v2, v3
	v_mul_hi_u32 v2, v1, v2
	v_mul_lo_u32 v3, v2, v0
	v_sub_u32_e32 v1, v1, v3
	v_add_u32_e32 v5, 1, v2
	v_cmp_ge_u32_e32 vcc, v1, v0
	v_sub_u32_e32 v3, v1, v0
	s_nop 0
	v_cndmask_b32_e32 v2, v2, v5, vcc
	v_cndmask_b32_e32 v1, v1, v3, vcc
	v_add_u32_e32 v3, 1, v2
	v_cmp_ge_u32_e32 vcc, v1, v0
	s_nop 1
	v_cndmask_b32_e32 v2, v2, v3, vcc
	v_mul_lo_u32 v1, v0, v2
	v_add_u32_e32 v0, v1, v0
	v_cmp_ne_u32_e32 vcc, v4, v0
	v_readfirstlane_b32 s98, v0
	v_mov_b64_e32 v[0:1], s[8:9]
	s_and_saveexec_b64 s[4:5], vcc
	s_cbranch_execz .LBB0_2643
	v_mov_b32_e32 v0, 0
	global_load_dword v1, v0, s[8:9] offset:-256 sc1
	s_mov_b64 s[14:15], 0
	s_waitcnt vmcnt(0)
	v_cmp_gt_u32_e32 vcc, s98, v1
	s_and_saveexec_b64 s[12:13], vcc
	s_cbranch_execz .LBB0_2642
	s_add_u32 s10, s72, 0x200
	s_addc_u32 s11, s73, 0
	s_mov_b32 s30, 1
	s_branch .LBB0_2635

.LBB0_2637:
	global_load_dword v1, v0, s[8:9] offset:-256 sc1
	s_add_i32 s30, s30, 1
	s_mov_b64 s[24:25], -1
	s_waitcnt vmcnt(0)
	v_cmp_le_u32_e32 vcc, s98, v1
	s_orn2_b64 s[28:29], vcc, exec
	s_branch .LBB0_2634

.LBB0_2721:
	s_or_b64 exec, exec, s[8:9]
	v_cvt_f32_u32_e32 v3, v0
	s_waitcnt vmcnt(0)
	v_readfirstlane_b32 s6, v2
	s_add_u32 s8, s72, 0x3500
	s_addc_u32 s9, s73, 0
	v_rcp_iflag_f32_e32 v3, v3
	v_add_u32_e32 v1, s6, v1
	v_add_u32_e32 v4, 1, v1
	s_mov_b64 s[10:11], -1
	v_mul_f32_e32 v2, 0x4f7ffffe, v3
	v_cvt_u32_f32_e32 v2, v2
	v_sub_u32_e32 v3, 0, v0
	v_mul_lo_u32 v3, v3, v2
	v_mul_hi_u32 v3, v2, v3
	v_add_u32_e32 v2, v2, v3
	v_mul_hi_u32 v2, v1, v2
	v_mul_lo_u32 v3, v2, v0
	v_sub_u32_e32 v1, v1, v3
	v_add_u32_e32 v5, 1, v2
	v_cmp_ge_u32_e32 vcc, v1, v0
	v_sub_u32_e32 v3, v1, v0
	s_nop 0
	v_cndmask_b32_e32 v2, v2, v5, vcc
	v_cndmask_b32_e32 v1, v1, v3, vcc
	v_add_u32_e32 v3, 1, v2
	v_cmp_ge_u32_e32 vcc, v1, v0
	s_nop 1
	v_cndmask_b32_e32 v2, v2, v3, vcc
	v_mul_lo_u32 v1, v0, v2
	v_add_u32_e32 v0, v1, v0
	v_cmp_ne_u32_e32 vcc, v4, v0
	v_readfirstlane_b32 s98, v0
	v_mov_b64_e32 v[0:1], s[8:9]
	s_and_saveexec_b64 s[6:7], vcc
	s_cbranch_execz .LBB0_2733
	v_mov_b32_e32 v0, 0
	global_load_dword v1, v0, s[8:9] offset:-256 sc1
	s_mov_b64 s[14:15], 0
	s_waitcnt vmcnt(0)
	v_cmp_gt_u32_e32 vcc, s98, v1
	s_and_saveexec_b64 s[12:13], vcc
	s_cbranch_execz .LBB0_2732
	s_add_u32 s10, s72, 0x200
	s_addc_u32 s11, s73, 0
	s_mov_b32 s30, 1
	s_branch .LBB0_2725

.LBB0_2979:
	s_or_b64 exec, exec, s[8:9]
	v_cvt_f32_u32_e32 v3, v0
	s_waitcnt vmcnt(0)
	v_readfirstlane_b32 s6, v2
	s_add_u32 s8, s72, 0x3500
	s_addc_u32 s9, s73, 0
	v_rcp_iflag_f32_e32 v3, v3
	v_add_u32_e32 v1, s6, v1
	v_add_u32_e32 v4, 1, v1
	s_mov_b64 s[10:11], -1
	v_mul_f32_e32 v2, 0x4f7ffffe, v3
	v_cvt_u32_f32_e32 v2, v2
	v_sub_u32_e32 v3, 0, v0
	v_mul_lo_u32 v3, v3, v2
	v_mul_hi_u32 v3, v2, v3
	v_add_u32_e32 v2, v2, v3
	v_mul_hi_u32 v2, v1, v2
	v_mul_lo_u32 v3, v2, v0
	v_sub_u32_e32 v1, v1, v3
	v_add_u32_e32 v5, 1, v2
	v_cmp_ge_u32_e32 vcc, v1, v0
	v_sub_u32_e32 v3, v1, v0
	s_nop 0
	v_cndmask_b32_e32 v2, v2, v5, vcc
	v_cndmask_b32_e32 v1, v1, v3, vcc
	v_add_u32_e32 v3, 1, v2
	v_cmp_ge_u32_e32 vcc, v1, v0
	s_nop 1
	v_cndmask_b32_e32 v2, v2, v3, vcc
	v_mul_lo_u32 v1, v0, v2
	v_add_u32_e32 v0, v1, v0
	v_cmp_ne_u32_e32 vcc, v4, v0
	v_readfirstlane_b32 s98, v0
	v_mov_b64_e32 v[0:1], s[8:9]
	s_and_saveexec_b64 s[6:7], vcc
	s_cbranch_execz .LBB0_2991
	v_mov_b32_e32 v0, 0
	global_load_dword v1, v0, s[8:9] offset:-256 sc1
	s_mov_b64 s[14:15], 0
	s_waitcnt vmcnt(0)
	v_cmp_gt_u32_e32 vcc, s98, v1
	s_and_saveexec_b64 s[12:13], vcc
	s_cbranch_execz .LBB0_2990
	s_add_u32 s10, s72, 0x200
	s_addc_u32 s11, s73, 0
	s_mov_b32 s24, 1
	s_branch .LBB0_2983

.LBB0_2985:
	global_load_dword v1, v0, s[8:9] offset:-256 sc1
	s_add_i32 s24, s24, 1
	s_mov_b64 s[18:19], -1
	s_waitcnt vmcnt(0)
	v_cmp_le_u32_e32 vcc, s98, v1
	s_orn2_b64 s[22:23], vcc, exec
	s_branch .LBB0_2982

.LBB0_3211:
	s_or_b64 exec, exec, s[6:7]
	v_cvt_f32_u32_e32 v3, v0
	s_waitcnt vmcnt(0)
	v_readfirstlane_b32 s4, v2
	s_add_u32 s6, s72, 0x3500
	s_addc_u32 s7, s73, 0
	v_rcp_iflag_f32_e32 v3, v3
	v_add_u32_e32 v1, s4, v1
	v_add_u32_e32 v4, 1, v1
	s_mov_b64 s[10:11], -1
	v_mul_f32_e32 v2, 0x4f7ffffe, v3
	v_cvt_u32_f32_e32 v2, v2
	v_sub_u32_e32 v3, 0, v0
	v_mul_lo_u32 v3, v3, v2
	v_mul_hi_u32 v3, v2, v3
	v_add_u32_e32 v2, v2, v3
	v_mul_hi_u32 v2, v1, v2
	v_mul_lo_u32 v3, v2, v0
	v_sub_u32_e32 v1, v1, v3
	v_add_u32_e32 v5, 1, v2
	v_cmp_ge_u32_e32 vcc, v1, v0
	v_sub_u32_e32 v3, v1, v0
	s_nop 0
	v_cndmask_b32_e32 v2, v2, v5, vcc
	v_cndmask_b32_e32 v1, v1, v3, vcc
	v_add_u32_e32 v3, 1, v2
	v_cmp_ge_u32_e32 vcc, v1, v0
	s_nop 1
	v_cndmask_b32_e32 v2, v2, v3, vcc
	v_mul_lo_u32 v1, v0, v2
	v_add_u32_e32 v0, v1, v0
	v_cmp_ne_u32_e32 vcc, v4, v0
	v_readfirstlane_b32 s98, v0
	v_mov_b64_e32 v[0:1], s[6:7]
	s_and_saveexec_b64 s[4:5], vcc
	s_cbranch_execz .LBB0_3223
	v_mov_b32_e32 v0, 0
	global_load_dword v1, v0, s[6:7] offset:-256 sc1
	s_mov_b64 s[14:15], 0
	s_waitcnt vmcnt(0)
	v_cmp_gt_u32_e32 vcc, s98, v1
	s_and_saveexec_b64 s[12:13], vcc
	s_cbranch_execz .LBB0_3222
	s_add_u32 s10, s72, 0x200
	s_addc_u32 s11, s73, 0
	s_mov_b32 s26, 1
	s_branch .LBB0_3215

.LBB0_3217:
	global_load_dword v1, v0, s[6:7] offset:-256 sc1
	s_add_i32 s26, s26, 1
	s_mov_b64 s[20:21], -1
	s_waitcnt vmcnt(0)
	v_cmp_le_u32_e32 vcc, s98, v1
	s_orn2_b64 s[24:25], vcc, exec
	s_branch .LBB0_3214

.LBB0_3379:
	s_or_b64 exec, exec, s[8:9]
	v_cvt_f32_u32_e32 v3, v0
	s_waitcnt vmcnt(0)
	v_readfirstlane_b32 s4, v2
	s_add_u32 s8, s72, 0x3500
	s_addc_u32 s9, s73, 0
	v_rcp_iflag_f32_e32 v3, v3
	v_add_u32_e32 v1, s4, v1
	v_add_u32_e32 v4, 1, v1
	s_mov_b64 s[10:11], -1
	v_mul_f32_e32 v2, 0x4f7ffffe, v3
	v_cvt_u32_f32_e32 v2, v2
	v_sub_u32_e32 v3, 0, v0
	v_mul_lo_u32 v3, v3, v2
	v_mul_hi_u32 v3, v2, v3
	v_add_u32_e32 v2, v2, v3
	v_mul_hi_u32 v2, v1, v2
	v_mul_lo_u32 v3, v2, v0
	v_sub_u32_e32 v1, v1, v3
	v_add_u32_e32 v5, 1, v2
	v_cmp_ge_u32_e32 vcc, v1, v0
	v_sub_u32_e32 v3, v1, v0
	s_nop 0
	v_cndmask_b32_e32 v2, v2, v5, vcc
	v_cndmask_b32_e32 v1, v1, v3, vcc
	v_add_u32_e32 v3, 1, v2
	v_cmp_ge_u32_e32 vcc, v1, v0
	s_nop 1
	v_cndmask_b32_e32 v2, v2, v3, vcc
	v_mul_lo_u32 v1, v0, v2
	v_add_u32_e32 v0, v1, v0
	v_cmp_ne_u32_e32 vcc, v4, v0
	v_readfirstlane_b32 s98, v0
	v_mov_b64_e32 v[0:1], s[8:9]
	s_and_saveexec_b64 s[4:5], vcc
	s_cbranch_execz .LBB0_3391
	v_mov_b32_e32 v0, 0
	global_load_dword v1, v0, s[8:9] offset:-256 sc1
	s_mov_b64 s[14:15], 0
	s_waitcnt vmcnt(0)
	v_cmp_gt_u32_e32 vcc, s98, v1
	s_and_saveexec_b64 s[12:13], vcc
	s_cbranch_execz .LBB0_3390
	s_add_u32 s10, s72, 0x200
	s_addc_u32 s11, s73, 0
	s_mov_b32 s28, 1
	s_branch .LBB0_3383

.LBB0_3385:
	global_load_dword v1, v0, s[8:9] offset:-256 sc1
	s_add_i32 s28, s28, 1
	s_mov_b64 s[22:23], -1
	s_waitcnt vmcnt(0)
	v_cmp_le_u32_e32 vcc, s98, v1
	s_orn2_b64 s[26:27], vcc, exec
	s_branch .LBB0_3382

.LBB0_3469:
	s_or_b64 exec, exec, s[8:9]
	v_cvt_f32_u32_e32 v3, v0
	s_waitcnt vmcnt(0)
	v_readfirstlane_b32 s6, v2
	s_add_u32 s8, s72, 0x3500
	s_addc_u32 s9, s73, 0
	v_rcp_iflag_f32_e32 v3, v3
	v_add_u32_e32 v1, s6, v1
	v_add_u32_e32 v4, 1, v1
	s_mov_b64 s[10:11], -1
	v_mul_f32_e32 v2, 0x4f7ffffe, v3
	v_cvt_u32_f32_e32 v2, v2
	v_sub_u32_e32 v3, 0, v0
	v_mul_lo_u32 v3, v3, v2
	v_mul_hi_u32 v3, v2, v3
	v_add_u32_e32 v2, v2, v3
	v_mul_hi_u32 v2, v1, v2
	v_mul_lo_u32 v3, v2, v0
	v_sub_u32_e32 v1, v1, v3
	v_add_u32_e32 v5, 1, v2
	v_cmp_ge_u32_e32 vcc, v1, v0
	v_sub_u32_e32 v3, v1, v0
	s_nop 0
	v_cndmask_b32_e32 v2, v2, v5, vcc
	v_cndmask_b32_e32 v1, v1, v3, vcc
	v_add_u32_e32 v3, 1, v2
	v_cmp_ge_u32_e32 vcc, v1, v0
	s_nop 1
	v_cndmask_b32_e32 v2, v2, v3, vcc
	v_mul_lo_u32 v1, v0, v2
	v_add_u32_e32 v0, v1, v0
	v_cmp_ne_u32_e32 vcc, v4, v0
	v_readfirstlane_b32 s98, v0
	v_mov_b64_e32 v[0:1], s[8:9]
	s_and_saveexec_b64 s[6:7], vcc
	s_cbranch_execz .LBB0_3481
	v_mov_b32_e32 v0, 0
	global_load_dword v1, v0, s[8:9] offset:-256 sc1
	s_mov_b64 s[14:15], 0
	s_waitcnt vmcnt(0)
	v_cmp_gt_u32_e32 vcc, s98, v1
	s_and_saveexec_b64 s[12:13], vcc
	s_cbranch_execz .LBB0_3480
	s_add_u32 s10, s72, 0x200
	s_addc_u32 s11, s73, 0
	s_mov_b32 s28, 1
	s_branch .LBB0_3473
